# speedup vs baseline: 1.0137x; 1.0137x over previous
.LBB1_15:
	s_and_b64 vcc, exec, s[4:5]
	s_cbranch_vccz .LBB1_54
	s_branch .Lmy_csr

.Lmy_csr:
	s_waitcnt lgkmcnt(0)
	s_load_dwordx8 s[4:11], s[0:1], 0x28
	s_load_dwordx8 s[12:19], s[0:1], 0x48
	s_sub_i32 s3, s2, 0xfc
	v_lshrrev_b32_e32 v1, 3, v0
	v_and_b32_e32 v2, 7, v0
	v_lshlrev_b32_e32 v8, 2, v0
	v_mov_b32_e32 v9, 0
	v_mov_b32_e32 v7, 1
	v_add_u32_e32 v10, 0x20000, v8
	ds_write_b32 v10, v9
	v_cmp_gt_u32_e32 vcc, 0x200, v0
	s_and_saveexec_b64 s[20:21], vcc
	v_add_u32_e32 v10, 0x22000, v8
	ds_write_b32 v10, v9
	ds_write_b32 v10, v9 offset:4096
	s_or_b64 exec, exec, s[20:21]
	v_cmp_eq_u32_e32 vcc, 0, v0
	s_and_saveexec_b64 s[20:21], vcc
	v_mov_b32_e32 v10, 0x21040
	ds_write_b32 v10, v9
	s_or_b64 exec, exec, s[20:21]
	s_lshl_b32 s22, s3, 9
	v_lshl_add_u32 v11, v1, 2, s22
	s_waitcnt lgkmcnt(0)
	global_load_dword v3, v11, s[4:5]
	global_load_dword v4, v11, s[4:5] offset:512
	global_load_dword v5, v11, s[6:7]
	global_load_dword v6, v11, s[6:7] offset:512
	s_barrier
	v_mul_u32_u24_e32 v12, 0x1e85, v1
	v_mov_b32_e32 v16, -1
	v_mov_b32_e32 v17, -1
	v_mov_b32_e32 v18, -1
	v_mov_b32_e32 v19, -1
	v_mov_b32_e32 v20, -1
	v_mov_b32_e32 v21, -1
	v_mov_b32_e32 v22, -1
	v_mov_b32_e32 v23, -1
	v_mov_b32_e32 v24, -1
	v_mov_b32_e32 v25, -1
	v_mov_b32_e32 v26, -1
	v_mov_b32_e32 v27, -1
	v_mov_b32_e32 v28, -1
	v_mov_b32_e32 v29, -1
	v_mov_b32_e32 v30, -1
	v_mov_b32_e32 v31, -1
	s_waitcnt vmcnt(0)
	v_cmp_eq_u32_e32 vcc, 0, v2
	s_and_saveexec_b64 s[20:21], vcc
	v_mov_b32_e32 v10, 0x21040
	ds_add_u32 v10, v3
	s_or_b64 exec, exec, s[20:21]
	v_add_u32_e32 v3, v3, v12
	v_add_u32_e32 v4, v4, v12
	v_add_u32_e32 v5, v5, v12
	v_add_u32_e32 v6, v6, v12
	v_add_u32_e32 v13, v3, v2
	v_add_u32_e32 v14, v5, v2
	v_lshlrev_b32_e32 v40, 2, v13
	v_lshlrev_b32_e32 v41, 2, v14
	v_add_u32_e32 v42, 0, v13
	v_cmp_lt_i32_e32 vcc, v42, v4
	s_and_saveexec_b64 s[20:21], vcc
	global_load_dword v16, v40, s[8:9] offset:0
	s_or_b64 exec, exec, s[20:21]
	v_add_u32_e32 v42, 8, v13
	v_cmp_lt_i32_e32 vcc, v42, v4
	s_and_saveexec_b64 s[20:21], vcc
	global_load_dword v17, v40, s[8:9] offset:32
	s_or_b64 exec, exec, s[20:21]
	v_add_u32_e32 v42, 16, v13
	v_cmp_lt_i32_e32 vcc, v42, v4
	s_and_saveexec_b64 s[20:21], vcc
	global_load_dword v18, v40, s[8:9] offset:64
	s_or_b64 exec, exec, s[20:21]
	v_add_u32_e32 v42, 24, v13
	v_cmp_lt_i32_e32 vcc, v42, v4
	s_and_saveexec_b64 s[20:21], vcc
	global_load_dword v19, v40, s[8:9] offset:96
	s_or_b64 exec, exec, s[20:21]
	v_add_u32_e32 v42, 32, v13
	v_cmp_lt_i32_e32 vcc, v42, v4
	s_and_saveexec_b64 s[20:21], vcc
	global_load_dword v20, v40, s[8:9] offset:128
	s_or_b64 exec, exec, s[20:21]
	v_add_u32_e32 v42, 40, v13
	v_cmp_lt_i32_e32 vcc, v42, v4
	s_and_saveexec_b64 s[20:21], vcc
	global_load_dword v21, v40, s[8:9] offset:160
	s_or_b64 exec, exec, s[20:21]
	v_add_u32_e32 v42, 48, v13
	v_cmp_lt_i32_e32 vcc, v42, v4
	s_and_saveexec_b64 s[20:21], vcc
	global_load_dword v22, v40, s[8:9] offset:192
	s_or_b64 exec, exec, s[20:21]
	v_add_u32_e32 v42, 56, v13
	v_cmp_lt_i32_e32 vcc, v42, v4
	s_and_saveexec_b64 s[20:21], vcc
	global_load_dword v23, v40, s[8:9] offset:224
	s_or_b64 exec, exec, s[20:21]
	v_add_u32_e32 v42, 0, v14
	v_cmp_lt_i32_e32 vcc, v42, v6
	s_and_saveexec_b64 s[20:21], vcc
	global_load_dword v24, v41, s[10:11] offset:0
	s_or_b64 exec, exec, s[20:21]
	v_add_u32_e32 v42, 8, v14
	v_cmp_lt_i32_e32 vcc, v42, v6
	s_and_saveexec_b64 s[20:21], vcc
	global_load_dword v25, v41, s[10:11] offset:32
	s_or_b64 exec, exec, s[20:21]
	v_add_u32_e32 v42, 16, v14
	v_cmp_lt_i32_e32 vcc, v42, v6
	s_and_saveexec_b64 s[20:21], vcc
	global_load_dword v26, v41, s[10:11] offset:64
	s_or_b64 exec, exec, s[20:21]
	v_add_u32_e32 v42, 24, v14
	v_cmp_lt_i32_e32 vcc, v42, v6
	s_and_saveexec_b64 s[20:21], vcc
	global_load_dword v27, v41, s[10:11] offset:96
	s_or_b64 exec, exec, s[20:21]
	v_add_u32_e32 v42, 32, v14
	v_cmp_lt_i32_e32 vcc, v42, v6
	s_and_saveexec_b64 s[20:21], vcc
	global_load_dword v28, v41, s[10:11] offset:128
	s_or_b64 exec, exec, s[20:21]
	v_add_u32_e32 v42, 40, v14
	v_cmp_lt_i32_e32 vcc, v42, v6
	s_and_saveexec_b64 s[20:21], vcc
	global_load_dword v29, v41, s[10:11] offset:160
	s_or_b64 exec, exec, s[20:21]
	v_add_u32_e32 v42, 48, v14
	v_cmp_lt_i32_e32 vcc, v42, v6
	s_and_saveexec_b64 s[20:21], vcc
	global_load_dword v30, v41, s[10:11] offset:192
	s_or_b64 exec, exec, s[20:21]
	v_add_u32_e32 v42, 56, v14
	v_cmp_lt_i32_e32 vcc, v42, v6
	s_and_saveexec_b64 s[20:21], vcc
	global_load_dword v31, v41, s[10:11] offset:224
	s_or_b64 exec, exec, s[20:21]
	s_waitcnt vmcnt(0)
	v_cmp_lt_i32_e32 vcc, -1, v16
	s_and_saveexec_b64 s[20:21], vcc
	v_lshrrev_b32_e32 v42, 15, v16
	v_and_b32_e32 v42, 0x7fc, v42
	v_add_u32_e32 v42, 0x22000, v42
	ds_add_rtn_u32 v32, v42, v7
	s_or_b64 exec, exec, s[20:21]
	v_cmp_lt_i32_e32 vcc, -1, v17
	s_and_saveexec_b64 s[20:21], vcc
	v_lshrrev_b32_e32 v42, 15, v17
	v_and_b32_e32 v42, 0x7fc, v42
	v_add_u32_e32 v42, 0x22000, v42
	ds_add_rtn_u32 v33, v42, v7
	s_or_b64 exec, exec, s[20:21]
	v_cmp_lt_i32_e32 vcc, -1, v18
	s_and_saveexec_b64 s[20:21], vcc
	v_lshrrev_b32_e32 v42, 15, v18
	v_and_b32_e32 v42, 0x7fc, v42
	v_add_u32_e32 v42, 0x22000, v42
	ds_add_rtn_u32 v34, v42, v7
	s_or_b64 exec, exec, s[20:21]
	v_cmp_lt_i32_e32 vcc, -1, v19
	s_and_saveexec_b64 s[20:21], vcc
	v_lshrrev_b32_e32 v42, 15, v19
	v_and_b32_e32 v42, 0x7fc, v42
	v_add_u32_e32 v42, 0x22000, v42
	ds_add_rtn_u32 v35, v42, v7
	s_or_b64 exec, exec, s[20:21]
	v_cmp_lt_i32_e32 vcc, -1, v20
	s_and_saveexec_b64 s[20:21], vcc
	v_lshrrev_b32_e32 v42, 15, v20
	v_and_b32_e32 v42, 0x7fc, v42
	v_add_u32_e32 v42, 0x22000, v42
	ds_add_rtn_u32 v36, v42, v7
	s_or_b64 exec, exec, s[20:21]
	v_cmp_lt_i32_e32 vcc, -1, v21
	s_and_saveexec_b64 s[20:21], vcc
	v_lshrrev_b32_e32 v42, 15, v21
	v_and_b32_e32 v42, 0x7fc, v42
	v_add_u32_e32 v42, 0x22000, v42
	ds_add_rtn_u32 v37, v42, v7
	s_or_b64 exec, exec, s[20:21]
	v_cmp_lt_i32_e32 vcc, -1, v22
	s_and_saveexec_b64 s[20:21], vcc
	v_lshrrev_b32_e32 v42, 15, v22
	v_and_b32_e32 v42, 0x7fc, v42
	v_add_u32_e32 v42, 0x22000, v42
	ds_add_rtn_u32 v38, v42, v7
	s_or_b64 exec, exec, s[20:21]
	v_cmp_lt_i32_e32 vcc, -1, v23
	s_and_saveexec_b64 s[20:21], vcc
	v_lshrrev_b32_e32 v42, 15, v23
	v_and_b32_e32 v42, 0x7fc, v42
	v_add_u32_e32 v42, 0x22000, v42
	ds_add_rtn_u32 v39, v42, v7
	s_or_b64 exec, exec, s[20:21]
	v_cmp_lt_i32_e32 vcc, -1, v24
	s_and_saveexec_b64 s[20:21], vcc
	v_lshlrev_b32_e32 v42, 2, v24
	v_add_u32_e32 v42, 0x23000, v42
	ds_add_u32 v42, v7
	s_or_b64 exec, exec, s[20:21]
	v_cmp_lt_i32_e32 vcc, -1, v25
	s_and_saveexec_b64 s[20:21], vcc
	v_lshlrev_b32_e32 v42, 2, v25
	v_add_u32_e32 v42, 0x23000, v42
	ds_add_u32 v42, v7
	s_or_b64 exec, exec, s[20:21]
	v_cmp_lt_i32_e32 vcc, -1, v26
	s_and_saveexec_b64 s[20:21], vcc
	v_lshlrev_b32_e32 v42, 2, v26
	v_add_u32_e32 v42, 0x23000, v42
	ds_add_u32 v42, v7
	s_or_b64 exec, exec, s[20:21]
	v_cmp_lt_i32_e32 vcc, -1, v27
	s_and_saveexec_b64 s[20:21], vcc
	v_lshlrev_b32_e32 v42, 2, v27
	v_add_u32_e32 v42, 0x23000, v42
	ds_add_u32 v42, v7
	s_or_b64 exec, exec, s[20:21]
	v_cmp_lt_i32_e32 vcc, -1, v28
	s_and_saveexec_b64 s[20:21], vcc
	v_lshlrev_b32_e32 v42, 2, v28
	v_add_u32_e32 v42, 0x23000, v42
	ds_add_u32 v42, v7
	s_or_b64 exec, exec, s[20:21]
	v_cmp_lt_i32_e32 vcc, -1, v29
	s_and_saveexec_b64 s[20:21], vcc
	v_lshlrev_b32_e32 v42, 2, v29
	v_add_u32_e32 v42, 0x23000, v42
	ds_add_u32 v42, v7
	s_or_b64 exec, exec, s[20:21]
	v_cmp_lt_i32_e32 vcc, -1, v30
	s_and_saveexec_b64 s[20:21], vcc
	v_lshlrev_b32_e32 v42, 2, v30
	v_add_u32_e32 v42, 0x23000, v42
	ds_add_u32 v42, v7
	s_or_b64 exec, exec, s[20:21]
	v_cmp_lt_i32_e32 vcc, -1, v31
	s_and_saveexec_b64 s[20:21], vcc
	v_lshlrev_b32_e32 v42, 2, v31
	v_add_u32_e32 v42, 0x23000, v42
	ds_add_u32 v42, v7
	s_or_b64 exec, exec, s[20:21]
	s_mov_b64 s[22:23], exec
	v_add_u32_e32 v43, 64, v13
.Lmy_rc1:
	v_cmp_lt_i32_e32 vcc, v43, v4
	s_and_b64 exec, exec, vcc
	s_cbranch_execz .Lmy_rc1d
	v_lshlrev_b32_e32 v44, 2, v43
	global_load_dword v45, v44, s[8:9]
	v_add_u32_e32 v43, 8, v43
	s_waitcnt vmcnt(0)
	v_lshrrev_b32_e32 v45, 15, v45
	v_and_b32_e32 v45, 0x7fc, v45
	v_add_u32_e32 v45, 0x20000, v45
	ds_add_u32 v45, v7
	s_branch .Lmy_rc1
.Lmy_rc1d:
	s_mov_b64 exec, s[22:23]
	v_add_u32_e32 v43, 64, v14
.Lmy_rc2:
	v_cmp_lt_i32_e32 vcc, v43, v6
	s_and_b64 exec, exec, vcc
	s_cbranch_execz .Lmy_rc2d
	v_lshlrev_b32_e32 v44, 2, v43
	global_load_dword v45, v44, s[10:11]
	v_add_u32_e32 v43, 8, v43
	s_waitcnt vmcnt(0)
	v_lshlrev_b32_e32 v45, 2, v45
	v_add_u32_e32 v45, 0x23000, v45
	ds_add_u32 v45, v7
	s_branch .Lmy_rc2
.Lmy_rc2d:
	s_mov_b64 exec, s[22:23]
	s_waitcnt lgkmcnt(0)
	s_barrier
	v_mbcnt_lo_u32_b32 v47, -1, 0
	v_mbcnt_hi_u32_b32 v47, -1, v47
	v_mov_b32_e32 v10, 0x21040
	ds_read_b32 v46, v10
	v_cmp_gt_u32_e32 vcc, 0x200, v0
	s_and_saveexec_b64 s[24:25], vcc
	s_cbranch_execz .Lmy_scan1d
	v_add_u32_e32 v10, 0x22000, v8
	ds_read_b32 v48, v10
	v_add_u32_e32 v10, 0x20000, v8
	ds_read_b32 v49, v10
	s_waitcnt lgkmcnt(0)
	v_add_u32_e32 v48, v48, v49
	v_mov_b32_e32 v51, v48
	v_cmp_le_u32_e32 vcc, 1, v47
	v_subrev_u32_e32 v49, 1, v47
	v_lshlrev_b32_e32 v49, 2, v49
	ds_bpermute_b32 v50, v49, v48
	s_waitcnt lgkmcnt(0)
	v_cndmask_b32_e32 v50, 0, v50, vcc
	v_add_u32_e32 v48, v48, v50
	v_cmp_le_u32_e32 vcc, 2, v47
	v_subrev_u32_e32 v49, 2, v47
	v_lshlrev_b32_e32 v49, 2, v49
	ds_bpermute_b32 v50, v49, v48
	s_waitcnt lgkmcnt(0)
	v_cndmask_b32_e32 v50, 0, v50, vcc
	v_add_u32_e32 v48, v48, v50
	v_cmp_le_u32_e32 vcc, 4, v47
	v_subrev_u32_e32 v49, 4, v47
	v_lshlrev_b32_e32 v49, 2, v49
	ds_bpermute_b32 v50, v49, v48
	s_waitcnt lgkmcnt(0)
	v_cndmask_b32_e32 v50, 0, v50, vcc
	v_add_u32_e32 v48, v48, v50
	v_cmp_le_u32_e32 vcc, 8, v47
	v_subrev_u32_e32 v49, 8, v47
	v_lshlrev_b32_e32 v49, 2, v49
	ds_bpermute_b32 v50, v49, v48
	s_waitcnt lgkmcnt(0)
	v_cndmask_b32_e32 v50, 0, v50, vcc
	v_add_u32_e32 v48, v48, v50
	v_cmp_le_u32_e32 vcc, 16, v47
	v_subrev_u32_e32 v49, 16, v47
	v_lshlrev_b32_e32 v49, 2, v49
	ds_bpermute_b32 v50, v49, v48
	s_waitcnt lgkmcnt(0)
	v_cndmask_b32_e32 v50, 0, v50, vcc
	v_add_u32_e32 v48, v48, v50
	v_cmp_le_u32_e32 vcc, 32, v47
	v_subrev_u32_e32 v49, 32, v47
	v_lshlrev_b32_e32 v49, 2, v49
	ds_bpermute_b32 v50, v49, v48
	s_waitcnt lgkmcnt(0)
	v_cndmask_b32_e32 v50, 0, v50, vcc
	v_add_u32_e32 v48, v48, v50
	v_lshrrev_b32_e32 v52, 6, v0
	v_lshlrev_b32_e32 v52, 2, v52
	v_add_u32_e32 v52, 0x21000, v52
	v_cmp_eq_u32_e32 vcc, 63, v47
	s_and_saveexec_b64 s[20:21], vcc
	ds_write_b32 v52, v48
	s_or_b64 exec, exec, s[20:21]
.Lmy_scan1d:
	s_or_b64 exec, exec, s[24:25]
	s_waitcnt lgkmcnt(0)
	s_barrier
	v_cmp_gt_u32_e32 vcc, 0x200, v0
	s_and_saveexec_b64 s[24:25], vcc
	s_cbranch_execz .Lmy_scan2d
	v_mov_b32_e32 v10, 0x21000
	ds_read_b128 v[52:55], v10
	ds_read_b128 v[56:59], v10 offset:16
	v_readfirstlane_b32 s26, v0
	s_nop 3
	s_lshr_b32 s26, s26, 6
	s_waitcnt lgkmcnt(0)
	v_mov_b32_e32 v60, 0
	s_cmp_gt_u32 s26, 0
	s_cselect_b64 vcc, -1, 0
	v_cndmask_b32_e32 v61, 0, v52, vcc
	v_add_u32_e32 v60, v60, v61
	s_cmp_gt_u32 s26, 1
	s_cselect_b64 vcc, -1, 0
	v_cndmask_b32_e32 v61, 0, v53, vcc
	v_add_u32_e32 v60, v60, v61
	s_cmp_gt_u32 s26, 2
	s_cselect_b64 vcc, -1, 0
	v_cndmask_b32_e32 v61, 0, v54, vcc
	v_add_u32_e32 v60, v60, v61
	s_cmp_gt_u32 s26, 3
	s_cselect_b64 vcc, -1, 0
	v_cndmask_b32_e32 v61, 0, v55, vcc
	v_add_u32_e32 v60, v60, v61
	s_cmp_gt_u32 s26, 4
	s_cselect_b64 vcc, -1, 0
	v_cndmask_b32_e32 v61, 0, v56, vcc
	v_add_u32_e32 v60, v60, v61
	s_cmp_gt_u32 s26, 5
	s_cselect_b64 vcc, -1, 0
	v_cndmask_b32_e32 v61, 0, v57, vcc
	v_add_u32_e32 v60, v60, v61
	s_cmp_gt_u32 s26, 6
	s_cselect_b64 vcc, -1, 0
	v_cndmask_b32_e32 v61, 0, v58, vcc
	v_add_u32_e32 v60, v60, v61
	v_add_u32_e32 v60, v60, v48
	v_sub_u32_e32 v60, v60, v51
	v_add_u32_e32 v10, 0x22800, v8
	ds_write_b32 v10, v60
	v_add_u32_e32 v10, 0x23000, v8
	ds_read_b32 v62, v10
	v_lshl_or_b32 v61, s3, 9, v0
	s_mov_b32 s27, 0x186a0
	v_cmp_gt_u32_e32 vcc, s27, v61
	s_and_saveexec_b64 s[20:21], vcc
	s_cbranch_execz .Lmy_scan3d
	v_lshlrev_b32_e32 v61, 2, v61
	v_add_u32_e32 v63, v46, v60
	global_store_dword v61, v63, s[12:13]
	global_store_dword v61, v51, s[14:15]
	s_waitcnt lgkmcnt(0)
	global_store_dword v61, v62, s[16:17]

.Lmy_scan2d:
	s_or_b64 exec, exec, s[24:25]
	s_waitcnt lgkmcnt(0)
	s_barrier
	v_cmp_lt_i32_e32 vcc, -1, v16
	s_and_saveexec_b64 s[20:21], vcc
	v_lshrrev_b32_e32 v42, 15, v16
	v_and_b32_e32 v42, 0x7fc, v42
	v_add_u32_e32 v42, 0x22800, v42
	ds_read_b32 v42, v42
	v_and_b32_e32 v16, 0x1ffff, v16
	s_waitcnt lgkmcnt(0)
	v_add_u32_e32 v42, v42, v32
	v_lshlrev_b32_e32 v42, 2, v42
	ds_write_b32 v42, v16
	s_or_b64 exec, exec, s[20:21]
	v_cmp_lt_i32_e32 vcc, -1, v17
	s_and_saveexec_b64 s[20:21], vcc
	v_lshrrev_b32_e32 v42, 15, v17
	v_and_b32_e32 v42, 0x7fc, v42
	v_add_u32_e32 v42, 0x22800, v42
	ds_read_b32 v42, v42
	v_and_b32_e32 v17, 0x1ffff, v17
	s_waitcnt lgkmcnt(0)
	v_add_u32_e32 v42, v42, v33
	v_lshlrev_b32_e32 v42, 2, v42
	ds_write_b32 v42, v17
	s_or_b64 exec, exec, s[20:21]
	v_cmp_lt_i32_e32 vcc, -1, v18
	s_and_saveexec_b64 s[20:21], vcc
	v_lshrrev_b32_e32 v42, 15, v18
	v_and_b32_e32 v42, 0x7fc, v42
	v_add_u32_e32 v42, 0x22800, v42
	ds_read_b32 v42, v42
	v_and_b32_e32 v18, 0x1ffff, v18
	s_waitcnt lgkmcnt(0)
	v_add_u32_e32 v42, v42, v34
	v_lshlrev_b32_e32 v42, 2, v42
	ds_write_b32 v42, v18
	s_or_b64 exec, exec, s[20:21]
	v_cmp_lt_i32_e32 vcc, -1, v19
	s_and_saveexec_b64 s[20:21], vcc
	v_lshrrev_b32_e32 v42, 15, v19
	v_and_b32_e32 v42, 0x7fc, v42
	v_add_u32_e32 v42, 0x22800, v42
	ds_read_b32 v42, v42
	v_and_b32_e32 v19, 0x1ffff, v19
	s_waitcnt lgkmcnt(0)
	v_add_u32_e32 v42, v42, v35
	v_lshlrev_b32_e32 v42, 2, v42
	ds_write_b32 v42, v19
	s_or_b64 exec, exec, s[20:21]
	v_cmp_lt_i32_e32 vcc, -1, v20
	s_and_saveexec_b64 s[20:21], vcc
	v_lshrrev_b32_e32 v42, 15, v20
	v_and_b32_e32 v42, 0x7fc, v42
	v_add_u32_e32 v42, 0x22800, v42
	ds_read_b32 v42, v42
	v_and_b32_e32 v20, 0x1ffff, v20
	s_waitcnt lgkmcnt(0)
	v_add_u32_e32 v42, v42, v36
	v_lshlrev_b32_e32 v42, 2, v42
	ds_write_b32 v42, v20
	s_or_b64 exec, exec, s[20:21]
	v_cmp_lt_i32_e32 vcc, -1, v21
	s_and_saveexec_b64 s[20:21], vcc
	v_lshrrev_b32_e32 v42, 15, v21
	v_and_b32_e32 v42, 0x7fc, v42
	v_add_u32_e32 v42, 0x22800, v42
	ds_read_b32 v42, v42
	v_and_b32_e32 v21, 0x1ffff, v21
	s_waitcnt lgkmcnt(0)
	v_add_u32_e32 v42, v42, v37
	v_lshlrev_b32_e32 v42, 2, v42
	ds_write_b32 v42, v21
	s_or_b64 exec, exec, s[20:21]
	v_cmp_lt_i32_e32 vcc, -1, v22
	s_and_saveexec_b64 s[20:21], vcc
	v_lshrrev_b32_e32 v42, 15, v22
	v_and_b32_e32 v42, 0x7fc, v42
	v_add_u32_e32 v42, 0x22800, v42
	ds_read_b32 v42, v42
	v_and_b32_e32 v22, 0x1ffff, v22
	s_waitcnt lgkmcnt(0)
	v_add_u32_e32 v42, v42, v38
	v_lshlrev_b32_e32 v42, 2, v42
	ds_write_b32 v42, v22
	s_or_b64 exec, exec, s[20:21]
	v_cmp_lt_i32_e32 vcc, -1, v23
	s_and_saveexec_b64 s[20:21], vcc
	v_lshrrev_b32_e32 v42, 15, v23
	v_and_b32_e32 v42, 0x7fc, v42
	v_add_u32_e32 v42, 0x22800, v42
	ds_read_b32 v42, v42
	v_and_b32_e32 v23, 0x1ffff, v23
	s_waitcnt lgkmcnt(0)
	v_add_u32_e32 v42, v42, v39
	v_lshlrev_b32_e32 v42, 2, v42
	ds_write_b32 v42, v23
	s_or_b64 exec, exec, s[20:21]
	s_mov_b64 s[22:23], exec
	v_add_u32_e32 v43, 64, v13
.Lmy_rc3:
	v_cmp_lt_i32_e32 vcc, v43, v4
	s_and_b64 exec, exec, vcc
	s_cbranch_execz .Lmy_rc3d
	v_lshlrev_b32_e32 v44, 2, v43
	global_load_dword v45, v44, s[8:9]
	v_add_u32_e32 v43, 8, v43
	s_waitcnt vmcnt(0)
	v_lshrrev_b32_e32 v44, 15, v45
	v_and_b32_e32 v44, 0x7fc, v44
	v_add_u32_e32 v42, 0x20800, v44
	ds_add_rtn_u32 v42, v42, v7
	v_add_u32_e32 v49, 0x22800, v44
	ds_read_b32 v49, v49
	v_add_u32_e32 v50, 0x22000, v44
	ds_read_b32 v50, v50
	v_and_b32_e32 v45, 0x1ffff, v45
	s_waitcnt lgkmcnt(0)
	v_add3_u32 v42, v42, v49, v50
	v_lshlrev_b32_e32 v42, 2, v42
	ds_write_b32 v42, v45
	s_branch .Lmy_rc3
.Lmy_rc3d:
	s_mov_b64 exec, s[22:23]
	s_waitcnt lgkmcnt(0)
	s_barrier
	v_mov_b32_e32 v2, 0x227fc
	v_mov_b32_e32 v3, 0x22ffc
	v_mov_b32_e32 v4, 0x207fc
	ds_read_b32 v2, v2
	ds_read_b32 v3, v3
	ds_read_b32 v4, v4
	v_mov_b32_e32 v9, v0
	s_mov_b64 s[24:25], 0x1000
	s_mov_b32 s21, 0
	s_waitcnt lgkmcnt(0)
	v_add3_u32 v2, v2, v3, v4
	v_add_u32_e32 v4, v46, v0
	v_ashrrev_i32_e32 v5, 31, v4
	v_lshl_add_u64 v[4:5], v[4:5], 2, s[18:19]
	v_readfirstlane_b32 s20, v2
	s_nop 3
